# K1 rank phase straight-line; payloads and counter addresses precomputed under load latency, scatter phase reads only
# baseline (speedup 1.0000x reference)
.LBB0_7:
	v_add_u32_e32 v1, 0x400, v1
	v_cmp_lt_u32_e32 vcc, s3, v1
	ds_write2st64_b32 v2, v3, v3 offset1:64
	s_or_b64 s[0:1], vcc, s[0:1]
	v_add_u32_e32 v2, 0x1000, v2
	s_andn2_b64 exec, exec, s[0:1]
	s_cbranch_execnz .LBB0_7
	s_or_b64 exec, exec, s[0:1]
	s_mul_i32 s34, s2, 0x30d4
	v_lshrrev_b32_e32 v53, 6, v0
	s_movk_i32 s0, 0x30e
	v_mov_b32_e32 v1, s34
	v_mad_u32_u24 v3, v53, s0, v1
	v_and_b32_e32 v2, 63, v0
	s_add_i32 s0, s34, 0x30d4
	v_add_u32_e32 v4, 0x30e, v3
	v_min_i32_e32 v8, s0, v4
	v_add_u32_e32 v3, v3, v2
	v_cmp_lt_i32_e64 s[22:23], v3, v8
	v_mov_b32_e32 v60, 0
	v_mov_b32_e32 v78, 0
	v_cndmask_b32_e64 v4, v1, v3, s[22:23]
	v_ashrrev_i32_e32 v5, 31, v4
	v_lshlrev_b64 v[4:5], 2, v[4:5]
	s_waitcnt lgkmcnt(0)
	v_lshl_add_u64 v[6:7], s[28:29], 0, v[4:5]
	v_lshl_add_u64 v[4:5], s[30:31], 0, v[4:5]
	global_load_dword v52, v[4:5], off nt
	v_add_u32_e32 v4, 64, v3
	v_cmp_lt_i32_e64 s[20:21], v4, v8
	global_load_dword v51, v[6:7], off nt
	v_mov_b32_e32 v79, 0
	v_cndmask_b32_e64 v4, v1, v4, s[20:21]
	v_ashrrev_i32_e32 v5, 31, v4
	v_lshlrev_b64 v[4:5], 2, v[4:5]
	v_lshl_add_u64 v[6:7], s[28:29], 0, v[4:5]
	v_lshl_add_u64 v[4:5], s[30:31], 0, v[4:5]
	global_load_dword v50, v[4:5], off nt
	v_add_u32_e32 v4, 0x80, v3
	v_cmp_lt_i32_e64 s[18:19], v4, v8
	global_load_dword v49, v[6:7], off nt
	s_nop 0
	v_cndmask_b32_e64 v4, v1, v4, s[18:19]
	v_ashrrev_i32_e32 v5, 31, v4
	v_lshlrev_b64 v[4:5], 2, v[4:5]
	v_lshl_add_u64 v[6:7], s[28:29], 0, v[4:5]
	v_lshl_add_u64 v[4:5], s[30:31], 0, v[4:5]
	global_load_dword v48, v[4:5], off nt
	v_add_u32_e32 v4, 0xc0, v3
	v_cmp_lt_i32_e64 s[16:17], v4, v8
	global_load_dword v47, v[6:7], off nt
	s_nop 0
	v_cndmask_b32_e64 v4, v1, v4, s[16:17]
	v_ashrrev_i32_e32 v5, 31, v4
	v_lshlrev_b64 v[4:5], 2, v[4:5]
	v_lshl_add_u64 v[6:7], s[28:29], 0, v[4:5]
	v_lshl_add_u64 v[4:5], s[30:31], 0, v[4:5]
	global_load_dword v46, v[4:5], off nt
	v_add_u32_e32 v4, 0x100, v3
	v_cmp_lt_i32_e64 s[14:15], v4, v8
	global_load_dword v45, v[6:7], off nt
	s_nop 0
	v_cndmask_b32_e64 v4, v1, v4, s[14:15]
	v_ashrrev_i32_e32 v5, 31, v4
	v_lshlrev_b64 v[4:5], 2, v[4:5]
	v_lshl_add_u64 v[6:7], s[28:29], 0, v[4:5]
	v_lshl_add_u64 v[4:5], s[30:31], 0, v[4:5]
	global_load_dword v44, v[4:5], off nt
	v_add_u32_e32 v4, 0x140, v3
	v_cmp_lt_i32_e64 s[12:13], v4, v8
	global_load_dword v43, v[6:7], off nt
	s_nop 0
	v_cndmask_b32_e64 v4, v1, v4, s[12:13]
	v_ashrrev_i32_e32 v5, 31, v4
	v_lshlrev_b64 v[4:5], 2, v[4:5]
	v_lshl_add_u64 v[6:7], s[28:29], 0, v[4:5]
	v_lshl_add_u64 v[4:5], s[30:31], 0, v[4:5]
	global_load_dword v42, v[4:5], off nt
	v_add_u32_e32 v4, 0x180, v3
	v_cmp_lt_i32_e64 s[10:11], v4, v8
	global_load_dword v41, v[6:7], off nt
	s_nop 0
	v_cndmask_b32_e64 v4, v1, v4, s[10:11]
	v_ashrrev_i32_e32 v5, 31, v4
	v_lshlrev_b64 v[4:5], 2, v[4:5]
	v_lshl_add_u64 v[6:7], s[28:29], 0, v[4:5]
	v_lshl_add_u64 v[4:5], s[30:31], 0, v[4:5]
	global_load_dword v40, v[4:5], off nt
	v_add_u32_e32 v4, 0x1c0, v3
	v_cmp_lt_i32_e64 s[8:9], v4, v8
	global_load_dword v39, v[6:7], off nt
	s_nop 0
	v_cndmask_b32_e64 v4, v1, v4, s[8:9]
	v_ashrrev_i32_e32 v5, 31, v4
	v_lshlrev_b64 v[4:5], 2, v[4:5]
	v_lshl_add_u64 v[6:7], s[28:29], 0, v[4:5]
	v_lshl_add_u64 v[4:5], s[30:31], 0, v[4:5]
	global_load_dword v38, v[4:5], off nt
	v_add_u32_e32 v4, 0x200, v3
	v_cmp_lt_i32_e64 s[6:7], v4, v8
	global_load_dword v37, v[6:7], off nt
	s_nop 0
	v_cndmask_b32_e64 v4, v1, v4, s[6:7]
	v_ashrrev_i32_e32 v5, 31, v4
	v_lshlrev_b64 v[4:5], 2, v[4:5]
	v_lshl_add_u64 v[6:7], s[28:29], 0, v[4:5]
	v_lshl_add_u64 v[4:5], s[30:31], 0, v[4:5]
	global_load_dword v36, v[4:5], off nt
	v_add_u32_e32 v4, 0x240, v3
	v_cmp_lt_i32_e64 s[4:5], v4, v8
	global_load_dword v35, v[6:7], off nt
	s_nop 0
	v_cndmask_b32_e64 v4, v1, v4, s[4:5]
	v_ashrrev_i32_e32 v5, 31, v4
	v_lshlrev_b64 v[4:5], 2, v[4:5]
	v_lshl_add_u64 v[6:7], s[28:29], 0, v[4:5]
	v_lshl_add_u64 v[4:5], s[30:31], 0, v[4:5]
	global_load_dword v34, v[4:5], off nt
	v_add_u32_e32 v4, 0x280, v3
	v_cmp_lt_i32_e64 s[24:25], v4, v8
	global_load_dword v33, v[6:7], off nt
	s_nop 0
	v_cndmask_b32_e64 v4, v1, v4, s[24:25]
	v_ashrrev_i32_e32 v5, 31, v4
	v_lshlrev_b64 v[4:5], 2, v[4:5]
	v_lshl_add_u64 v[6:7], s[28:29], 0, v[4:5]
	v_lshl_add_u64 v[4:5], s[30:31], 0, v[4:5]
	global_load_dword v32, v[4:5], off nt
	v_add_u32_e32 v4, 0x2c0, v3
	v_cmp_lt_i32_e64 s[0:1], v4, v8
	v_add_u32_e32 v3, 0x300, v3
	global_load_dword v31, v[6:7], off nt
	v_cndmask_b32_e64 v4, v1, v4, s[0:1]
	v_ashrrev_i32_e32 v5, 31, v4
	v_lshlrev_b64 v[4:5], 2, v[4:5]
	v_lshl_add_u64 v[6:7], s[28:29], 0, v[4:5]
	v_lshl_add_u64 v[4:5], s[30:31], 0, v[4:5]
	v_cmp_lt_i32_e32 vcc, v3, v8
	global_load_dword v30, v[4:5], off nt
	global_load_dword v28, v[6:7], off nt
	v_cndmask_b32_e32 v4, v1, v3, vcc
	v_ashrrev_i32_e32 v5, 31, v4
	v_lshlrev_b64 v[4:5], 2, v[4:5]
	v_lshl_add_u64 v[6:7], s[28:29], 0, v[4:5]
	v_lshl_add_u64 v[4:5], s[30:31], 0, v[4:5]
	global_load_dword v1, v[6:7], off nt
	global_load_dword v26, v[4:5], off nt
	v_lshlrev_b32_e32 v3, 10, v53
	v_add_u32_e32 v27, 0x12500, v3
	v_add_u32_e32 v29, 0x16500, v3
	s_barrier
	s_mov_b64 s[44:45], exec
	s_mov_b32 s46, 0x51eb851f
	s_movk_i32 s47, 0x7e70
	s_mov_b32 s48, 0xfe70
	v_mov_b32_e32 v6, 1
	s_and_b64 exec, s[44:45], s[22:23]
	s_waitcnt vmcnt(25)
	v_mul_hi_u32 v4, v52, s46
	v_lshrrev_b32_e32 v4, 7, v4
	v_lshl_add_u32 v98, v4, 2, v27
	ds_add_rtn_u32 v78, v98, v6
	s_waitcnt vmcnt(24)
	v_mul_hi_u32 v5, v51, s46
	v_lshrrev_b32_e32 v5, 7, v5
	v_lshl_add_u32 v97, v5, 2, v29
	ds_add_rtn_u32 v79, v97, v6
	v_mad_u32_u24 v4, v4, s47, v52
	v_lshl_or_b32 v52, v4, 17, v51
	v_mad_u32_u24 v51, v5, s48, v51
	s_and_b64 exec, s[44:45], s[20:21]
	s_waitcnt vmcnt(23)
	v_mul_hi_u32 v4, v50, s46
	v_lshrrev_b32_e32 v4, 7, v4
	v_lshl_add_u32 v100, v4, 2, v27
	ds_add_rtn_u32 v77, v100, v6
	s_waitcnt vmcnt(22)
	v_mul_hi_u32 v5, v49, s46
	v_lshrrev_b32_e32 v5, 7, v5
	v_lshl_add_u32 v99, v5, 2, v29
	ds_add_rtn_u32 v60, v99, v6
	v_mad_u32_u24 v4, v4, s47, v50
	v_lshl_or_b32 v50, v4, 17, v49
	v_mad_u32_u24 v49, v5, s48, v49
	s_and_b64 exec, s[44:45], s[18:19]
	s_waitcnt vmcnt(21)
	v_mul_hi_u32 v4, v48, s46
	v_lshrrev_b32_e32 v4, 7, v4
	v_lshl_add_u32 v102, v4, 2, v27
	ds_add_rtn_u32 v76, v102, v6
	s_waitcnt vmcnt(20)
	v_mul_hi_u32 v5, v47, s46
	v_lshrrev_b32_e32 v5, 7, v5
	v_lshl_add_u32 v101, v5, 2, v29
	ds_add_rtn_u32 v75, v101, v6
	v_mad_u32_u24 v4, v4, s47, v48
	v_lshl_or_b32 v48, v4, 17, v47
	v_mad_u32_u24 v47, v5, s48, v47
	s_and_b64 exec, s[44:45], s[16:17]
	s_waitcnt vmcnt(19)
	v_mul_hi_u32 v4, v46, s46
	v_lshrrev_b32_e32 v4, 7, v4
	v_lshl_add_u32 v104, v4, 2, v27
	ds_add_rtn_u32 v74, v104, v6
	s_waitcnt vmcnt(18)
	v_mul_hi_u32 v5, v45, s46
	v_lshrrev_b32_e32 v5, 7, v5
	v_lshl_add_u32 v103, v5, 2, v29
	ds_add_rtn_u32 v58, v103, v6
	v_mad_u32_u24 v4, v4, s47, v46
	v_lshl_or_b32 v46, v4, 17, v45
	v_mad_u32_u24 v45, v5, s48, v45
	s_and_b64 exec, s[44:45], s[14:15]
	s_waitcnt vmcnt(17)
	v_mul_hi_u32 v4, v44, s46
	v_lshrrev_b32_e32 v4, 7, v4
	v_lshl_add_u32 v106, v4, 2, v27
	ds_add_rtn_u32 v73, v106, v6
	s_waitcnt vmcnt(16)
	v_mul_hi_u32 v5, v43, s46
	v_lshrrev_b32_e32 v5, 7, v5
	v_lshl_add_u32 v105, v5, 2, v29
	ds_add_rtn_u32 v72, v105, v6
	v_mad_u32_u24 v4, v4, s47, v44
	v_lshl_or_b32 v44, v4, 17, v43
	v_mad_u32_u24 v43, v5, s48, v43
	s_and_b64 exec, s[44:45], s[12:13]
	s_waitcnt vmcnt(15)
	v_mul_hi_u32 v4, v42, s46
	v_lshrrev_b32_e32 v4, 7, v4
	v_lshl_add_u32 v108, v4, 2, v27
	ds_add_rtn_u32 v71, v108, v6
	s_waitcnt vmcnt(14)
	v_mul_hi_u32 v5, v41, s46
	v_lshrrev_b32_e32 v5, 7, v5
	v_lshl_add_u32 v107, v5, 2, v29
	ds_add_rtn_u32 v57, v107, v6
	v_mad_u32_u24 v4, v4, s47, v42
	v_lshl_or_b32 v42, v4, 17, v41
	v_mad_u32_u24 v41, v5, s48, v41
	s_and_b64 exec, s[44:45], s[10:11]
	s_waitcnt vmcnt(13)
	v_mul_hi_u32 v4, v40, s46
	v_lshrrev_b32_e32 v4, 7, v4
	v_lshl_add_u32 v110, v4, 2, v27
	ds_add_rtn_u32 v70, v110, v6
	s_waitcnt vmcnt(12)
	v_mul_hi_u32 v5, v39, s46
	v_lshrrev_b32_e32 v5, 7, v5
	v_lshl_add_u32 v109, v5, 2, v29
	ds_add_rtn_u32 v69, v109, v6
	v_mad_u32_u24 v4, v4, s47, v40
	v_lshl_or_b32 v40, v4, 17, v39
	v_mad_u32_u24 v39, v5, s48, v39
	s_and_b64 exec, s[44:45], s[8:9]
	s_waitcnt vmcnt(11)
	v_mul_hi_u32 v4, v38, s46
	v_lshrrev_b32_e32 v4, 7, v4
	v_lshl_add_u32 v112, v4, 2, v27
	ds_add_rtn_u32 v68, v112, v6
	s_waitcnt vmcnt(10)
	v_mul_hi_u32 v5, v37, s46
	v_lshrrev_b32_e32 v5, 7, v5
	v_lshl_add_u32 v111, v5, 2, v29
	ds_add_rtn_u32 v56, v111, v6
	v_mad_u32_u24 v4, v4, s47, v38
	v_lshl_or_b32 v38, v4, 17, v37
	v_mad_u32_u24 v37, v5, s48, v37
	s_and_b64 exec, s[44:45], s[6:7]
	s_waitcnt vmcnt(9)
	v_mul_hi_u32 v4, v36, s46
	v_lshrrev_b32_e32 v4, 7, v4
	v_lshl_add_u32 v114, v4, 2, v27
	ds_add_rtn_u32 v67, v114, v6
	s_waitcnt vmcnt(8)
	v_mul_hi_u32 v5, v35, s46
	v_lshrrev_b32_e32 v5, 7, v5
	v_lshl_add_u32 v113, v5, 2, v29
	ds_add_rtn_u32 v66, v113, v6
	v_mad_u32_u24 v4, v4, s47, v36
	v_lshl_or_b32 v36, v4, 17, v35
	v_mad_u32_u24 v35, v5, s48, v35
	s_and_b64 exec, s[44:45], s[4:5]
	s_waitcnt vmcnt(7)
	v_mul_hi_u32 v4, v34, s46
	v_lshrrev_b32_e32 v4, 7, v4
	v_lshl_add_u32 v116, v4, 2, v27
	ds_add_rtn_u32 v65, v116, v6
	s_waitcnt vmcnt(6)
	v_mul_hi_u32 v5, v33, s46
	v_lshrrev_b32_e32 v5, 7, v5
	v_lshl_add_u32 v115, v5, 2, v29
	ds_add_rtn_u32 v55, v115, v6
	v_mad_u32_u24 v4, v4, s47, v34
	v_lshl_or_b32 v34, v4, 17, v33
	v_mad_u32_u24 v33, v5, s48, v33
	s_and_b64 exec, s[44:45], s[24:25]
	s_waitcnt vmcnt(5)
	v_mul_hi_u32 v4, v32, s46
	v_lshrrev_b32_e32 v4, 7, v4
	v_lshl_add_u32 v118, v4, 2, v27
	ds_add_rtn_u32 v64, v118, v6
	s_waitcnt vmcnt(4)
	v_mul_hi_u32 v5, v31, s46
	v_lshrrev_b32_e32 v5, 7, v5
	v_lshl_add_u32 v117, v5, 2, v29
	ds_add_rtn_u32 v63, v117, v6
	v_mad_u32_u24 v4, v4, s47, v32
	v_lshl_or_b32 v32, v4, 17, v31
	v_mad_u32_u24 v31, v5, s48, v31
	s_and_b64 exec, s[44:45], s[0:1]
	s_waitcnt vmcnt(3)
	v_mul_hi_u32 v4, v30, s46
	v_lshrrev_b32_e32 v4, 7, v4
	v_lshl_add_u32 v120, v4, 2, v27
	ds_add_rtn_u32 v62, v120, v6
	s_waitcnt vmcnt(2)
	v_mul_hi_u32 v5, v28, s46
	v_lshrrev_b32_e32 v5, 7, v5
	v_lshl_add_u32 v119, v5, 2, v29
	ds_add_rtn_u32 v54, v119, v6
	v_mad_u32_u24 v4, v4, s47, v30
	v_lshl_or_b32 v30, v4, 17, v28
	v_mad_u32_u24 v28, v5, s48, v28
	s_and_b64 exec, s[44:45], vcc
	s_waitcnt vmcnt(0)
	v_mul_hi_u32 v4, v26, s46
	v_lshrrev_b32_e32 v4, 7, v4
	v_lshl_add_u32 v122, v4, 2, v27
	ds_add_rtn_u32 v61, v122, v6
	v_mul_hi_u32 v5, v1, s46
	v_lshrrev_b32_e32 v5, 7, v5
	v_lshl_add_u32 v121, v5, 2, v29
	ds_add_rtn_u32 v59, v121, v6
	v_mad_u32_u24 v4, v4, s47, v26
	v_lshl_or_b32 v26, v4, 17, v1
	v_mad_u32_u24 v1, v5, s48, v1
	s_mov_b64 exec, s[44:45]
	v_and_b32_e32 v82, 3, v0
	v_and_b32_e32 v3, 0x3fc, v0
	v_lshl_or_b32 v3, v82, 12, v3
	v_add_u32_e32 v80, 0x12500, v3
	s_waitcnt lgkmcnt(0)
	s_barrier
	ds_read2st64_b32 v[18:19], v80 offset1:4
	v_add_u32_e32 v81, 0x16500, v3
	ds_read2st64_b32 v[20:21], v80 offset0:8 offset1:12
	ds_read2st64_b32 v[24:25], v81 offset1:4
	ds_read2st64_b32 v[22:23], v81 offset0:8 offset1:12
	s_waitcnt lgkmcnt(3)
	v_add_u32_e32 v3, v19, v18
	s_waitcnt lgkmcnt(1)
	v_add_u32_e32 v4, v25, v24
	v_add3_u32 v3, v3, v20, v21
	s_waitcnt lgkmcnt(0)
	v_add3_u32 v4, v4, v22, v23
	v_lshl_or_b32 v21, v4, 16, v3
	v_mov_b32_e32 v23, v21
	s_nop 1
	v_add_u32_dpp v23, v23, v23 row_shr:1 row_mask:0xf bank_mask:0xf
	s_nop 1
	v_add_u32_dpp v23, v23, v23 row_shr:2 row_mask:0xf bank_mask:0xf
	s_nop 1
	v_add_u32_dpp v23, v23, v23 row_shr:4 row_mask:0xf bank_mask:0xf
	s_nop 1
	v_add_u32_dpp v23, v23, v23 row_shr:8 row_mask:0xf bank_mask:0xf
	s_nop 1
	v_add_u32_dpp v23, v23, v23 row_bcast:15 row_mask:0xa bank_mask:0xf
	s_nop 1
	v_add_u32_dpp v23, v23, v23 row_bcast:31 row_mask:0xc bank_mask:0xf
	v_cmp_eq_u32_e64 s[26:27], 63, v2
	s_and_saveexec_b64 s[28:29], s[26:27]
	v_mov_b32_e32 v2, 0x1a500
	v_lshl_or_b32 v2, v53, 2, v2
	ds_write_b32 v2, v23
	s_or_b64 exec, exec, s[28:29]
	v_mov_b32_e32 v2, 0x1a500
	s_waitcnt lgkmcnt(0)
	s_barrier
	ds_read_b128 v[2:5], v2
	v_mov_b32_e32 v6, 0x1a510
	ds_read_b128 v[6:9], v6
	v_cmp_lt_u32_e64 s[26:27], 63, v0
	s_movk_i32 s3, 0x7f
	v_mov_b32_e32 v10, 0x1a520
	s_waitcnt lgkmcnt(1)
	v_cndmask_b32_e64 v83, 0, v2, s[26:27]
	v_cmp_lt_u32_e64 s[26:27], s3, v0
	s_movk_i32 s3, 0xbf
	ds_read_b128 v[10:13], v10
	v_cndmask_b32_e64 v84, 0, v3, s[26:27]
	v_cmp_lt_u32_e64 s[26:27], s3, v0
	s_movk_i32 s3, 0xff
	v_mov_b32_e32 v14, 0x1a530
	v_cndmask_b32_e64 v85, 0, v4, s[26:27]
	v_cmp_lt_u32_e64 s[26:27], s3, v0
	s_movk_i32 s3, 0x13f
	ds_read_b128 v[14:17], v14
	v_cndmask_b32_e64 v86, 0, v5, s[26:27]
	v_cmp_lt_u32_e64 s[26:27], s3, v0
	s_movk_i32 s3, 0x17f
	v_sub_u32_e32 v21, v23, v21
	s_waitcnt lgkmcnt(2)
	v_cndmask_b32_e64 v87, 0, v6, s[26:27]
	v_cmp_lt_u32_e64 s[26:27], s3, v0
	s_movk_i32 s3, 0x1bf
	v_add_u32_e32 v21, v83, v21
	v_cndmask_b32_e64 v88, 0, v7, s[26:27]
	v_cmp_lt_u32_e64 s[26:27], s3, v0
	s_movk_i32 s3, 0x1ff
	v_add3_u32 v21, v21, v84, v85
	v_cndmask_b32_e64 v89, 0, v8, s[26:27]
	v_cmp_lt_u32_e64 s[26:27], s3, v0
	s_movk_i32 s3, 0x23f
	v_add3_u32 v21, v21, v86, v87
	v_cndmask_b32_e64 v90, 0, v9, s[26:27]
	v_cmp_lt_u32_e64 s[26:27], s3, v0
	s_movk_i32 s3, 0x27f
	v_add3_u32 v21, v21, v88, v89
	s_waitcnt lgkmcnt(1)
	v_cndmask_b32_e64 v91, 0, v10, s[26:27]
	v_cmp_lt_u32_e64 s[26:27], s3, v0
	s_movk_i32 s3, 0x2bf
	v_add3_u32 v21, v21, v90, v91
	v_cndmask_b32_e64 v92, 0, v11, s[26:27]
	v_cmp_lt_u32_e64 s[26:27], s3, v0
	s_movk_i32 s3, 0x2ff
	s_mul_i32 s28, s2, 0x101
	v_cndmask_b32_e64 v93, 0, v12, s[26:27]
	v_cmp_lt_u32_e64 s[26:27], s3, v0
	s_movk_i32 s3, 0x33f
	v_add3_u32 v21, v21, v92, v93
	v_cndmask_b32_e64 v94, 0, v13, s[26:27]
	v_cmp_lt_u32_e64 s[26:27], s3, v0
	s_movk_i32 s3, 0x37f
	s_waitcnt lgkmcnt(0)
	v_cndmask_b32_e64 v95, 0, v14, s[26:27]
	v_cmp_lt_u32_e64 s[26:27], s3, v0
	v_add3_u32 v21, v21, v94, v95
	s_nop 0
	v_cndmask_b32_e64 v96, 0, v15, s[26:27]
	v_cmp_eq_u32_e64 s[26:27], 15, v53
	s_nop 1
	v_cndmask_b32_e64 v53, 0, v16, s[26:27]
	v_add3_u32 v21, v21, v96, v53
	v_and_b32_e32 v23, 0xffff, v21
	v_lshrrev_b32_e32 v21, 16, v21
	v_cmp_eq_u32_e64 s[26:27], 0, v82
	s_and_saveexec_b64 s[30:31], s[26:27]
	s_cbranch_execz .LBB0_38
	v_lshrrev_b32_e32 v53, 2, v0
	v_add_u32_e32 v82, s28, v53
	v_ashrrev_i32_e32 v83, 31, v82
	v_lshlrev_b64 v[82:83], 2, v[82:83]
	v_lshl_add_u64 v[84:85], s[40:41], 0, v[82:83]
	v_lshl_add_u64 v[82:83], s[42:43], 0, v[82:83]
	global_store_dword v[84:85], v23, off
	global_store_dword v[82:83], v21, off

.LBB0_40:
	s_or_b64 exec, exec, s[30:31]
	v_add_u32_e32 v2, v18, v23
	v_add_u32_e32 v3, v24, v21
	ds_write2st64_b32 v80, v23, v2 offset1:4
	v_add_u32_e32 v2, v19, v2
	ds_write2st64_b32 v81, v21, v3 offset1:4
	v_add_u32_e32 v3, v25, v3
	v_add_u32_e32 v4, v20, v2
	v_add_u32_e32 v5, v22, v3
	ds_write2st64_b32 v80, v2, v4 offset0:8 offset1:12
	ds_write2st64_b32 v81, v3, v5 offset0:8 offset1:12
	s_waitcnt lgkmcnt(0)
	s_barrier
	s_mov_b64 s[44:45], exec
	s_and_b64 exec, s[44:45], s[22:23]
	ds_read_b32 v97, v97
	ds_read_b32 v98, v98
	s_and_b64 exec, s[44:45], s[20:21]
	ds_read_b32 v99, v99
	ds_read_b32 v100, v100
	s_and_b64 exec, s[44:45], s[18:19]
	ds_read_b32 v101, v101
	ds_read_b32 v102, v102
	s_and_b64 exec, s[44:45], s[16:17]
	ds_read_b32 v103, v103
	ds_read_b32 v104, v104
	s_and_b64 exec, s[44:45], s[14:15]
	ds_read_b32 v105, v105
	ds_read_b32 v106, v106
	s_and_b64 exec, s[44:45], s[12:13]
	ds_read_b32 v107, v107
	ds_read_b32 v108, v108
	s_and_b64 exec, s[44:45], s[10:11]
	ds_read_b32 v109, v109
	ds_read_b32 v110, v110
	s_and_b64 exec, s[44:45], s[22:23]
	s_waitcnt lgkmcnt(12)
	v_add_u32_e32 v5, v98, v78
	v_lshlrev_b32_e32 v5, 2, v5
	ds_write_b32 v5, v52
	v_add_u32_e32 v3, v97, v79
	v_lshlrev_b32_e32 v3, 1, v3
	ds_write_b16 v3, v51 offset:50000
	s_and_b64 exec, s[44:45], s[20:21]
	s_waitcnt lgkmcnt(12)
	v_add_u32_e32 v5, v100, v77
	v_lshlrev_b32_e32 v5, 2, v5
	ds_write_b32 v5, v50
	v_add_u32_e32 v3, v99, v60
	v_lshlrev_b32_e32 v3, 1, v3
	ds_write_b16 v3, v49 offset:50000
	s_and_b64 exec, s[44:45], s[18:19]
	s_waitcnt lgkmcnt(12)
	v_add_u32_e32 v5, v102, v76
	v_lshlrev_b32_e32 v5, 2, v5
	ds_write_b32 v5, v48
	v_add_u32_e32 v3, v101, v75
	v_lshlrev_b32_e32 v3, 1, v3
	ds_write_b16 v3, v47 offset:50000
	s_and_b64 exec, s[44:45], s[16:17]
	s_waitcnt lgkmcnt(12)
	v_add_u32_e32 v5, v104, v74
	v_lshlrev_b32_e32 v5, 2, v5
	ds_write_b32 v5, v46
	v_add_u32_e32 v3, v103, v58
	v_lshlrev_b32_e32 v3, 1, v3
	ds_write_b16 v3, v45 offset:50000
	s_and_b64 exec, s[44:45], s[14:15]
	s_waitcnt lgkmcnt(12)
	v_add_u32_e32 v5, v106, v73
	v_lshlrev_b32_e32 v5, 2, v5
	ds_write_b32 v5, v44
	v_add_u32_e32 v3, v105, v72
	v_lshlrev_b32_e32 v3, 1, v3
	ds_write_b16 v3, v43 offset:50000
	s_and_b64 exec, s[44:45], s[12:13]
	s_waitcnt lgkmcnt(12)
	v_add_u32_e32 v5, v108, v71
	v_lshlrev_b32_e32 v5, 2, v5
	ds_write_b32 v5, v42
	v_add_u32_e32 v3, v107, v57
	v_lshlrev_b32_e32 v3, 1, v3
	ds_write_b16 v3, v41 offset:50000
	s_and_b64 exec, s[44:45], s[10:11]
	s_waitcnt lgkmcnt(12)
	v_add_u32_e32 v5, v110, v70
	v_lshlrev_b32_e32 v5, 2, v5
	ds_write_b32 v5, v40
	v_add_u32_e32 v3, v109, v69
	v_lshlrev_b32_e32 v3, 1, v3
	ds_write_b16 v3, v39 offset:50000
	s_waitcnt lgkmcnt(2)
	s_and_b64 exec, s[44:45], s[8:9]
	ds_read_b32 v111, v111
	ds_read_b32 v112, v112
	s_and_b64 exec, s[44:45], s[6:7]
	ds_read_b32 v113, v113
	ds_read_b32 v114, v114
	s_and_b64 exec, s[44:45], s[4:5]
	ds_read_b32 v115, v115
	ds_read_b32 v116, v116
	s_and_b64 exec, s[44:45], s[24:25]
	ds_read_b32 v117, v117
	ds_read_b32 v118, v118
	s_and_b64 exec, s[44:45], s[0:1]
	ds_read_b32 v119, v119
	ds_read_b32 v120, v120
	s_and_b64 exec, s[44:45], vcc
	ds_read_b32 v121, v121
	ds_read_b32 v122, v122
	s_and_b64 exec, s[44:45], s[8:9]
	s_waitcnt lgkmcnt(10)
	v_add_u32_e32 v5, v112, v68
	v_lshlrev_b32_e32 v5, 2, v5
	ds_write_b32 v5, v38
	v_add_u32_e32 v3, v111, v56
	v_lshlrev_b32_e32 v3, 1, v3
	ds_write_b16 v3, v37 offset:50000
	s_and_b64 exec, s[44:45], s[6:7]
	s_waitcnt lgkmcnt(10)
	v_add_u32_e32 v5, v114, v67
	v_lshlrev_b32_e32 v5, 2, v5
	ds_write_b32 v5, v36
	v_add_u32_e32 v3, v113, v66
	v_lshlrev_b32_e32 v3, 1, v3
	ds_write_b16 v3, v35 offset:50000
	s_and_b64 exec, s[44:45], s[4:5]
	s_waitcnt lgkmcnt(10)
	v_add_u32_e32 v5, v116, v65
	v_lshlrev_b32_e32 v5, 2, v5
	ds_write_b32 v5, v34
	v_add_u32_e32 v3, v115, v55
	v_lshlrev_b32_e32 v3, 1, v3
	ds_write_b16 v3, v33 offset:50000
	s_and_b64 exec, s[44:45], s[24:25]
	s_waitcnt lgkmcnt(10)
	v_add_u32_e32 v5, v118, v64
	v_lshlrev_b32_e32 v5, 2, v5
	ds_write_b32 v5, v32
	v_add_u32_e32 v3, v117, v63
	v_lshlrev_b32_e32 v3, 1, v3
	ds_write_b16 v3, v31 offset:50000
	s_and_b64 exec, s[44:45], s[0:1]
	s_waitcnt lgkmcnt(10)
	v_add_u32_e32 v5, v120, v62
	v_lshlrev_b32_e32 v5, 2, v5
	ds_write_b32 v5, v30
	v_add_u32_e32 v3, v119, v54
	v_lshlrev_b32_e32 v3, 1, v3
	ds_write_b16 v3, v28 offset:50000
	s_and_b64 exec, s[44:45], vcc
	s_waitcnt lgkmcnt(10)
	v_add_u32_e32 v5, v122, v61
	v_lshlrev_b32_e32 v5, 2, v5
	ds_write_b32 v5, v26
	v_add_u32_e32 v3, v121, v59
	v_lshlrev_b32_e32 v3, 1, v3
	ds_write_b16 v3, v1 offset:50000
